# speedup vs baseline: 1.0415x; 1.0096x over previous
.LBB8_12:
	ds_read_b128 v[146:149], v188
	ds_read_b128 v[150:153], v188 offset:1024
	ds_read_b128 v[154:157], v188 offset:2048
	ds_read_b128 v[158:161], v188 offset:3072
	ds_read_b128 v[226:229], v190
	ds_read_b128 v[230:233], v190 offset:1024
	ds_read_b128 v[234:237], v190 offset:2048
	ds_read_b128 v[238:241], v190 offset:3072
	s_cmp_eq_u32 s51, s61
	s_cselect_b64 s[66:67], -1, 0
	s_add_i32 s61, s61, 2
	s_and_b64 s[34:35], s[66:67], exec
	s_cselect_b32 s35, s31, s60
	s_cselect_b32 s34, s30, s59
	s_cselect_b32 s64, s37, s57
	s_lshl_b32 s65, s64, 13
	s_and_b64 s[66:67], s[66:67], exec
	s_cselect_b32 s63, 0, s62
	s_add_i32 s68, s65, s63
	ds_read_b128 v[194:197], v189
	ds_read_b128 v[198:201], v189 offset:1024
	ds_read_b128 v[202:205], v189 offset:2048
	ds_read_b128 v[206:209], v189 offset:3072
	ds_read_b128 v[210:213], v189 offset:4096
	ds_read_b128 v[214:217], v189 offset:5120
	ds_read_b128 v[218:221], v189 offset:6144
	ds_read_b128 v[222:225], v189 offset:7168
	s_ashr_i32 s69, s68, 31
	s_waitcnt vmcnt(0)
	s_lshl_b64 s[66:67], s[68:69], 1
	v_pk_add_f16 v14, v14, v10
	v_pk_add_f16 v15, v15, v11
	v_pk_add_f16 v16, v16, v12
	v_pk_add_f16 v17, v17, v13
	s_add_u32 s70, s8, s66
	v_pk_max_f16 v17, v17, 0
	v_pk_max_f16 v16, v16, 0
	v_pk_max_f16 v15, v15, 0
	v_pk_max_f16 v14, v14, 0
	v_pk_add_f16 v6, v6, v10
	v_pk_add_f16 v7, v7, v11
	v_pk_add_f16 v8, v8, v12
	v_pk_add_f16 v9, v9, v13
	s_addc_u32 s71, s9, s67
	s_add_i32 s68, s68, s65
	v_pk_max_f16 v9, v9, 0
	v_pk_max_f16 v8, v8, 0
	v_pk_max_f16 v7, v7, 0
	v_pk_max_f16 v6, v6, 0
	ds_write_b128 v186, v[14:17] offset:49152
	ds_write_b128 v186, v[6:9] offset:57344
	s_ashr_i32 s69, s68, 31
	s_lshl_b32 s66, s64, 14
	s_lshl_b64 s[68:69], s[68:69], 1
	s_nop 4
	global_load_dwordx4 v[6:9], v184, s[70:71]
	s_add_u32 s68, s10, s68
	global_load_dwordx4 v[10:13], v185, s[70:71]
	s_addc_u32 s69, s11, s69
	global_load_dwordx4 v[14:17], v183, s[68:69]
	s_waitcnt lgkmcnt(2)
	s_barrier
	s_waitcnt lgkmcnt(0)
	s_setprio 1
	s_waitcnt lgkmcnt(0)
	v_mfma_f32_16x16x32_f16 v[138:141], v[146:149], v[194:197], v[138:141]
	v_mfma_f32_16x16x32_f16 v[142:145], v[154:157], v[194:197], v[142:145]
	v_mfma_f32_16x16x32_f16 v[126:129], v[146:149], v[202:205], v[126:129]
	v_mfma_f32_16x16x32_f16 v[122:125], v[154:157], v[202:205], v[122:125]
	v_mfma_f32_16x16x32_f16 v[110:113], v[146:149], v[210:213], v[110:113]
	v_mfma_f32_16x16x32_f16 v[106:109], v[154:157], v[210:213], v[106:109]
	v_mfma_f32_16x16x32_f16 v[94:97], v[146:149], v[218:221], v[94:97]
	v_mfma_f32_16x16x32_f16 v[90:93], v[154:157], v[218:221], v[90:93]
	v_mfma_f32_16x16x32_f16 v[138:141], v[150:153], v[198:201], v[138:141]
	v_mfma_f32_16x16x32_f16 v[142:145], v[158:161], v[198:201], v[142:145]
	v_mfma_f32_16x16x32_f16 v[126:129], v[150:153], v[206:209], v[126:129]
	v_mfma_f32_16x16x32_f16 v[122:125], v[158:161], v[206:209], v[122:125]
	v_mfma_f32_16x16x32_f16 v[110:113], v[150:153], v[214:217], v[110:113]
	v_mfma_f32_16x16x32_f16 v[106:109], v[158:161], v[214:217], v[106:109]
	v_mfma_f32_16x16x32_f16 v[94:97], v[150:153], v[222:225], v[94:97]
	v_mfma_f32_16x16x32_f16 v[90:93], v[158:161], v[222:225], v[90:93]
	s_setprio 0
	s_waitcnt lgkmcnt(0)
	s_setprio 1
	s_waitcnt lgkmcnt(0)
	v_mfma_f32_16x16x32_f16 v[134:137], v[226:229], v[194:197], v[134:137]
	v_mfma_f32_16x16x32_f16 v[130:133], v[234:237], v[194:197], v[130:133]
	v_mfma_f32_16x16x32_f16 v[118:121], v[226:229], v[202:205], v[118:121]
	v_mfma_f32_16x16x32_f16 v[114:117], v[234:237], v[202:205], v[114:117]
	v_mfma_f32_16x16x32_f16 v[102:105], v[226:229], v[210:213], v[102:105]
	v_mfma_f32_16x16x32_f16 v[98:101], v[234:237], v[210:213], v[98:101]
	v_mfma_f32_16x16x32_f16 v[86:89], v[226:229], v[218:221], v[86:89]
	v_mfma_f32_16x16x32_f16 v[82:85], v[234:237], v[218:221], v[82:85]
	v_mfma_f32_16x16x32_f16 v[134:137], v[230:233], v[198:201], v[134:137]
	v_mfma_f32_16x16x32_f16 v[130:133], v[238:241], v[198:201], v[130:133]
	v_mfma_f32_16x16x32_f16 v[118:121], v[230:233], v[206:209], v[118:121]
	v_mfma_f32_16x16x32_f16 v[114:117], v[238:241], v[206:209], v[114:117]
	v_mfma_f32_16x16x32_f16 v[102:105], v[230:233], v[214:217], v[102:105]
	v_mfma_f32_16x16x32_f16 v[98:101], v[238:241], v[214:217], v[98:101]
	v_mfma_f32_16x16x32_f16 v[86:89], v[230:233], v[222:225], v[86:89]
	v_mfma_f32_16x16x32_f16 v[82:85], v[238:241], v[222:225], v[82:85]
	s_setprio 0
	s_or_b32 s64, s65, 0x1000
	s_add_i32 s68, s64, s63
	s_barrier
	s_add_i32 s81, s53, s45
	v_lshl_add_u64 v[170:171], s[34:35], 0, v[162:163]
	s_mov_b32 m0, s81
	global_load_lds_dwordx4 v[170:171], off
	v_lshl_add_u64 v[242:243], s[34:35], 0, v[164:165]
	s_add_i32 m0, s81, 0x2000
	s_nop 0
	global_load_lds_dwordx4 v[242:243], off
	s_add_u32 s34, s34, s22
	s_addc_u32 s35, s35, s23
	s_add_i32 s82, s54, s45
	v_lshl_add_u64 v[244:245], s[34:35], 0, v[162:163]
	s_mov_b32 m0, s82
	v_lshl_add_u64 v[246:247], s[34:35], 0, v[164:165]
	global_load_lds_dwordx4 v[244:245], off
	s_add_i32 m0, s82, 0x2000
	s_nop 0
	global_load_lds_dwordx4 v[246:247], off
	ds_read_b128 v[194:197], v189 offset:16384
	ds_read_b128 v[198:201], v189 offset:17408
	ds_read_b128 v[202:205], v189 offset:18432
	ds_read_b128 v[206:209], v189 offset:19456
	ds_read_b128 v[210:213], v189 offset:20480
	ds_read_b128 v[214:217], v189 offset:21504
	ds_read_b128 v[218:221], v189 offset:22528
	ds_read_b128 v[222:225], v189 offset:23552
	s_ashr_i32 s69, s68, 31
	s_lshl_b64 s[68:69], s[68:69], 1
	s_waitcnt vmcnt(4)
	s_add_u32 s68, s8, s68
	v_pk_add_f16 v6, v6, v14
	v_pk_add_f16 v7, v7, v15
	v_pk_add_f16 v8, v8, v16
	v_pk_add_f16 v9, v9, v17
	s_addc_u32 s69, s9, s69
	s_or_b32 s67, s66, 0x2000
	v_pk_max_f16 v9, v9, 0
	v_pk_max_f16 v8, v8, 0
	v_pk_max_f16 v7, v7, 0
	v_pk_max_f16 v6, v6, 0
	v_pk_add_f16 v10, v10, v14
	v_pk_add_f16 v11, v11, v15
	v_pk_add_f16 v12, v12, v16
	v_pk_add_f16 v13, v13, v17
	s_add_i32 s70, s67, s63
	v_pk_max_f16 v13, v13, 0
	v_pk_max_f16 v12, v12, 0
	v_pk_max_f16 v11, v11, 0
	v_pk_max_f16 v10, v10, 0
	ds_write_b128 v186, v[6:9]
	ds_write_b128 v186, v[10:13] offset:8192
	s_ashr_i32 s71, s70, 31
	s_lshl_b64 s[70:71], s[70:71], 1
	s_nop 4
	global_load_dwordx4 v[6:9], v184, s[68:69]
	s_add_u32 s70, s10, s70
	global_load_dwordx4 v[10:13], v185, s[68:69]
	s_addc_u32 s71, s11, s71
	global_load_dwordx4 v[14:17], v183, s[70:71]
	s_waitcnt lgkmcnt(2)
	s_barrier
	s_waitcnt lgkmcnt(0)
	s_setprio 1
	s_waitcnt lgkmcnt(0)
	v_mfma_f32_16x16x32_f16 v[78:81], v[146:149], v[194:197], v[78:81]
	v_mfma_f32_16x16x32_f16 v[74:77], v[154:157], v[194:197], v[74:77]
	v_mfma_f32_16x16x32_f16 v[62:65], v[146:149], v[202:205], v[62:65]
	v_mfma_f32_16x16x32_f16 v[58:61], v[154:157], v[202:205], v[58:61]
	v_mfma_f32_16x16x32_f16 v[46:49], v[146:149], v[210:213], v[46:49]
	v_mfma_f32_16x16x32_f16 v[42:45], v[154:157], v[210:213], v[42:45]
	v_mfma_f32_16x16x32_f16 v[30:33], v[146:149], v[218:221], v[30:33]
	v_mfma_f32_16x16x32_f16 v[26:29], v[154:157], v[218:221], v[26:29]
	v_mfma_f32_16x16x32_f16 v[78:81], v[150:153], v[198:201], v[78:81]
	v_mfma_f32_16x16x32_f16 v[74:77], v[158:161], v[198:201], v[74:77]
	v_mfma_f32_16x16x32_f16 v[62:65], v[150:153], v[206:209], v[62:65]
	v_mfma_f32_16x16x32_f16 v[58:61], v[158:161], v[206:209], v[58:61]
	v_mfma_f32_16x16x32_f16 v[46:49], v[150:153], v[214:217], v[46:49]
	v_mfma_f32_16x16x32_f16 v[42:45], v[158:161], v[214:217], v[42:45]
	v_mfma_f32_16x16x32_f16 v[30:33], v[150:153], v[222:225], v[30:33]
	v_mfma_f32_16x16x32_f16 v[26:29], v[158:161], v[222:225], v[26:29]
	s_setprio 0
	s_setprio 1
	v_mfma_f32_16x16x32_f16 v[70:73], v[226:229], v[194:197], v[70:73]
	v_mfma_f32_16x16x32_f16 v[66:69], v[234:237], v[194:197], v[66:69]
	v_mfma_f32_16x16x32_f16 v[54:57], v[226:229], v[202:205], v[54:57]
	v_mfma_f32_16x16x32_f16 v[50:53], v[234:237], v[202:205], v[50:53]
	v_mfma_f32_16x16x32_f16 v[38:41], v[226:229], v[210:213], v[38:41]
	v_mfma_f32_16x16x32_f16 v[34:37], v[234:237], v[210:213], v[34:37]
	v_mfma_f32_16x16x32_f16 v[22:25], v[226:229], v[218:221], v[22:25]
	v_mfma_f32_16x16x32_f16 v[18:21], v[234:237], v[218:221], v[18:21]
	v_mfma_f32_16x16x32_f16 v[70:73], v[230:233], v[198:201], v[70:73]
	v_mfma_f32_16x16x32_f16 v[66:69], v[238:241], v[198:201], v[66:69]
	v_mfma_f32_16x16x32_f16 v[54:57], v[230:233], v[206:209], v[54:57]
	v_mfma_f32_16x16x32_f16 v[50:53], v[238:241], v[206:209], v[50:53]
	v_mfma_f32_16x16x32_f16 v[38:41], v[230:233], v[214:217], v[38:41]
	v_mfma_f32_16x16x32_f16 v[34:37], v[238:241], v[214:217], v[34:37]
	v_mfma_f32_16x16x32_f16 v[22:25], v[230:233], v[222:225], v[22:25]
	v_mfma_f32_16x16x32_f16 v[18:21], v[238:241], v[222:225], v[18:21]
	s_setprio 0
	s_barrier
	ds_read_b128 v[146:149], v191
	ds_read_b128 v[150:153], v191 offset:1024
	ds_read_b128 v[154:157], v191 offset:2048
	ds_read_b128 v[158:161], v191 offset:3072
	ds_read_b128 v[226:229], v192
	ds_read_b128 v[230:233], v192 offset:1024
	ds_read_b128 v[234:237], v192 offset:2048
	ds_read_b128 v[238:241], v192 offset:3072
	s_or_b32 s70, s63, 64
	s_ashr_i32 s35, s65, 31
	s_ashr_i32 s69, s63, 31
	s_add_u32 s34, s63, s65
	s_addc_u32 s35, s69, s35
	s_lshl_b64 s[34:35], s[34:35], 1
	s_add_u32 s34, s8, s34
	s_addc_u32 s35, s9, s35
	s_add_u32 s34, s34, 0x80
	ds_read_b128 v[194:197], v189 offset:32768
	ds_read_b128 v[198:201], v189 offset:33792
	ds_read_b128 v[202:205], v189 offset:34816
	ds_read_b128 v[206:209], v189 offset:35840
	ds_read_b128 v[210:213], v189 offset:36864
	ds_read_b128 v[214:217], v189 offset:37888
	ds_read_b128 v[218:221], v189 offset:38912
	ds_read_b128 v[222:225], v189 offset:39936
	s_addc_u32 s35, s35, 0
	s_ashr_i32 s65, s66, 31
	s_waitcnt vmcnt(0)
	s_add_u32 s68, s63, s66
	v_pk_add_f16 v6, v6, v14
	v_pk_add_f16 v7, v7, v15
	v_pk_add_f16 v8, v8, v16
	v_pk_add_f16 v9, v9, v17
	s_addc_u32 s69, s69, s65
	v_pk_max_f16 v9, v9, 0
	v_pk_max_f16 v8, v8, 0
	v_pk_max_f16 v7, v7, 0
	v_pk_max_f16 v6, v6, 0
	v_pk_add_f16 v10, v10, v14
	v_pk_add_f16 v11, v11, v15
	v_pk_add_f16 v12, v12, v16
	v_pk_add_f16 v13, v13, v17
	s_lshl_b64 s[68:69], s[68:69], 1
	v_pk_max_f16 v13, v13, 0
	v_pk_max_f16 v12, v12, 0
	v_pk_max_f16 v11, v11, 0
	v_pk_max_f16 v10, v10, 0
	ds_write_b128 v186, v[6:9] offset:16384
	ds_write_b128 v186, v[10:13] offset:24576
	s_add_u32 s63, s10, s68
	s_addc_u32 s65, s11, s69
	s_nop 4
	global_load_dwordx4 v[6:9], v184, s[34:35]
	s_add_u32 s68, s63, 0x80
	global_load_dwordx4 v[10:13], v185, s[34:35]
	s_addc_u32 s69, s65, 0
	global_load_dwordx4 v[14:17], v183, s[68:69]
	s_waitcnt lgkmcnt(2)
	s_barrier
	s_waitcnt lgkmcnt(0)
	s_setprio 1
	s_waitcnt lgkmcnt(0)
	v_mfma_f32_16x16x32_f16 v[138:141], v[146:149], v[194:197], v[138:141]
	v_mfma_f32_16x16x32_f16 v[142:145], v[154:157], v[194:197], v[142:145]
	v_mfma_f32_16x16x32_f16 v[126:129], v[146:149], v[202:205], v[126:129]
	v_mfma_f32_16x16x32_f16 v[122:125], v[154:157], v[202:205], v[122:125]
	v_mfma_f32_16x16x32_f16 v[110:113], v[146:149], v[210:213], v[110:113]
	v_mfma_f32_16x16x32_f16 v[106:109], v[154:157], v[210:213], v[106:109]
	v_mfma_f32_16x16x32_f16 v[94:97], v[146:149], v[218:221], v[94:97]
	v_mfma_f32_16x16x32_f16 v[90:93], v[154:157], v[218:221], v[90:93]
	v_mfma_f32_16x16x32_f16 v[138:141], v[150:153], v[198:201], v[138:141]
	v_mfma_f32_16x16x32_f16 v[142:145], v[158:161], v[198:201], v[142:145]
	v_mfma_f32_16x16x32_f16 v[126:129], v[150:153], v[206:209], v[126:129]
	v_mfma_f32_16x16x32_f16 v[122:125], v[158:161], v[206:209], v[122:125]
	v_mfma_f32_16x16x32_f16 v[110:113], v[150:153], v[214:217], v[110:113]
	v_mfma_f32_16x16x32_f16 v[106:109], v[158:161], v[214:217], v[106:109]
	v_mfma_f32_16x16x32_f16 v[94:97], v[150:153], v[222:225], v[94:97]
	v_mfma_f32_16x16x32_f16 v[90:93], v[158:161], v[222:225], v[90:93]
	s_setprio 0
	s_waitcnt lgkmcnt(0)
	s_setprio 1
	s_waitcnt lgkmcnt(0)
	v_mfma_f32_16x16x32_f16 v[134:137], v[226:229], v[194:197], v[134:137]
	v_mfma_f32_16x16x32_f16 v[130:133], v[234:237], v[194:197], v[130:133]
	v_mfma_f32_16x16x32_f16 v[118:121], v[226:229], v[202:205], v[118:121]
	v_mfma_f32_16x16x32_f16 v[114:117], v[234:237], v[202:205], v[114:117]
	v_mfma_f32_16x16x32_f16 v[102:105], v[226:229], v[210:213], v[102:105]
	v_mfma_f32_16x16x32_f16 v[98:101], v[234:237], v[210:213], v[98:101]
	v_mfma_f32_16x16x32_f16 v[86:89], v[226:229], v[218:221], v[86:89]
	v_mfma_f32_16x16x32_f16 v[82:85], v[234:237], v[218:221], v[82:85]
	v_mfma_f32_16x16x32_f16 v[134:137], v[230:233], v[198:201], v[134:137]
	v_mfma_f32_16x16x32_f16 v[130:133], v[238:241], v[198:201], v[130:133]
	v_mfma_f32_16x16x32_f16 v[118:121], v[230:233], v[206:209], v[118:121]
	v_mfma_f32_16x16x32_f16 v[114:117], v[238:241], v[206:209], v[114:117]
	v_mfma_f32_16x16x32_f16 v[102:105], v[230:233], v[214:217], v[102:105]
	v_mfma_f32_16x16x32_f16 v[98:101], v[238:241], v[214:217], v[98:101]
	v_mfma_f32_16x16x32_f16 v[86:89], v[230:233], v[222:225], v[86:89]
	v_mfma_f32_16x16x32_f16 v[82:85], v[238:241], v[222:225], v[82:85]
	s_setprio 0
	s_barrier
	s_add_i32 s81, s55, s45
	v_lshl_add_u64 v[170:171], v[170:171], 0, s[26:27]
	s_mov_b32 m0, s81
	global_load_lds_dwordx4 v[170:171], off
	v_lshl_add_u64 v[170:171], v[242:243], 0, s[26:27]
	s_add_i32 m0, s81, 0x2000
	s_nop 0
	global_load_lds_dwordx4 v[170:171], off
	s_add_i32 s82, s56, s45
	v_lshl_add_u64 v[248:249], v[244:245], 0, s[26:27]
	s_mov_b32 m0, s82
	s_nop 0
	global_load_lds_dwordx4 v[248:249], off
	v_lshl_add_u64 v[248:249], v[246:247], 0, s[26:27]
	s_add_i32 m0, s82, 0x2000
	s_nop 0
	global_load_lds_dwordx4 v[248:249], off
	ds_read_b128 v[194:197], v189 offset:49152
	ds_read_b128 v[198:201], v189 offset:50176
	ds_read_b128 v[202:205], v189 offset:51200
	ds_read_b128 v[206:209], v189 offset:52224
	ds_read_b128 v[210:213], v189 offset:53248
	ds_read_b128 v[214:217], v189 offset:54272
	ds_read_b128 v[218:221], v189 offset:55296
	ds_read_b128 v[222:225], v189 offset:56320
	s_add_i32 s34, s64, s70
	s_ashr_i32 s35, s34, 31
	s_waitcnt vmcnt(4)
	s_lshl_b64 s[34:35], s[34:35], 1
	v_pk_add_f16 v6, v6, v14
	v_pk_add_f16 v7, v7, v15
	v_pk_add_f16 v8, v8, v16
	v_pk_add_f16 v9, v9, v17
	s_add_u32 s34, s8, s34
	v_pk_max_f16 v9, v9, 0
	v_pk_max_f16 v8, v8, 0
	v_pk_max_f16 v7, v7, 0
	v_pk_max_f16 v6, v6, 0
	v_pk_add_f16 v10, v10, v14
	v_pk_add_f16 v11, v11, v15
	v_pk_add_f16 v12, v12, v16
	v_pk_add_f16 v13, v13, v17
	s_addc_u32 s35, s9, s35
	s_add_i32 s64, s67, s70
	v_pk_max_f16 v13, v13, 0
	v_pk_max_f16 v12, v12, 0
	v_pk_max_f16 v11, v11, 0
	v_pk_max_f16 v10, v10, 0
	ds_write_b128 v186, v[6:9] offset:32768
	ds_write_b128 v186, v[10:13] offset:40960
	s_ashr_i32 s65, s64, 31
	s_lshl_b64 s[64:65], s[64:65], 1
	s_nop 4
	global_load_dwordx4 v[14:17], v184, s[34:35]
	s_add_u32 s64, s10, s64
	global_load_dwordx4 v[6:9], v185, s[34:35]
	s_addc_u32 s65, s11, s65
	global_load_dwordx4 v[10:13], v183, s[64:65]
	s_waitcnt lgkmcnt(2)
	s_barrier
	s_waitcnt lgkmcnt(0)
	s_setprio 1
	s_waitcnt lgkmcnt(0)
	v_mfma_f32_16x16x32_f16 v[78:81], v[146:149], v[194:197], v[78:81]
	v_mfma_f32_16x16x32_f16 v[74:77], v[154:157], v[194:197], v[74:77]
	v_mfma_f32_16x16x32_f16 v[62:65], v[146:149], v[202:205], v[62:65]
	v_mfma_f32_16x16x32_f16 v[58:61], v[154:157], v[202:205], v[58:61]
	v_mfma_f32_16x16x32_f16 v[46:49], v[146:149], v[210:213], v[46:49]
	v_mfma_f32_16x16x32_f16 v[42:45], v[154:157], v[210:213], v[42:45]
	v_mfma_f32_16x16x32_f16 v[30:33], v[146:149], v[218:221], v[30:33]
	v_mfma_f32_16x16x32_f16 v[26:29], v[154:157], v[218:221], v[26:29]
	v_mfma_f32_16x16x32_f16 v[78:81], v[150:153], v[198:201], v[78:81]
	v_mfma_f32_16x16x32_f16 v[74:77], v[158:161], v[198:201], v[74:77]
	v_mfma_f32_16x16x32_f16 v[62:65], v[150:153], v[206:209], v[62:65]
	v_mfma_f32_16x16x32_f16 v[58:61], v[158:161], v[206:209], v[58:61]
	v_mfma_f32_16x16x32_f16 v[46:49], v[150:153], v[214:217], v[46:49]
	v_mfma_f32_16x16x32_f16 v[42:45], v[158:161], v[214:217], v[42:45]
	v_mfma_f32_16x16x32_f16 v[30:33], v[150:153], v[222:225], v[30:33]
	v_mfma_f32_16x16x32_f16 v[26:29], v[158:161], v[222:225], v[26:29]
	s_setprio 0
	s_setprio 1
	v_mfma_f32_16x16x32_f16 v[70:73], v[226:229], v[194:197], v[70:73]
	v_mfma_f32_16x16x32_f16 v[66:69], v[234:237], v[194:197], v[66:69]
	v_mfma_f32_16x16x32_f16 v[54:57], v[226:229], v[202:205], v[54:57]
	v_mfma_f32_16x16x32_f16 v[50:53], v[234:237], v[202:205], v[50:53]
	v_mfma_f32_16x16x32_f16 v[38:41], v[226:229], v[210:213], v[38:41]
	v_mfma_f32_16x16x32_f16 v[34:37], v[234:237], v[210:213], v[34:37]
	v_mfma_f32_16x16x32_f16 v[22:25], v[226:229], v[218:221], v[22:25]
	v_mfma_f32_16x16x32_f16 v[18:21], v[234:237], v[218:221], v[18:21]
	v_mfma_f32_16x16x32_f16 v[70:73], v[230:233], v[198:201], v[70:73]
	v_mfma_f32_16x16x32_f16 v[66:69], v[238:241], v[198:201], v[66:69]
	v_mfma_f32_16x16x32_f16 v[54:57], v[230:233], v[206:209], v[54:57]
	v_mfma_f32_16x16x32_f16 v[50:53], v[238:241], v[206:209], v[50:53]
	v_mfma_f32_16x16x32_f16 v[38:41], v[230:233], v[214:217], v[38:41]
	v_mfma_f32_16x16x32_f16 v[34:37], v[238:241], v[214:217], v[34:37]
	v_mfma_f32_16x16x32_f16 v[22:25], v[230:233], v[222:225], v[22:25]
	v_mfma_f32_16x16x32_f16 v[18:21], v[238:241], v[222:225], v[18:21]
	s_setprio 0
	s_addk_i32 s62, 0x80
	s_add_u32 s59, s59, 0x100
	s_addc_u32 s60, s60, 0
	s_cmp_ge_i32 s61, s49
	s_barrier
	s_cbranch_scc0 .LBB8_12
	s_branch .LBB8_20

.LBB8_37:
	ds_read_b128 v[144:147], v173
	ds_read_b128 v[148:151], v173 offset:1024
	ds_read_b128 v[152:155], v173 offset:2048
	ds_read_b128 v[156:159], v173 offset:3072
	ds_read_b128 v[212:215], v177
	ds_read_b128 v[216:219], v177 offset:1024
	ds_read_b128 v[220:223], v177 offset:2048
	ds_read_b128 v[224:227], v177 offset:3072
	s_cmp_eq_u32 s49, s61
	s_cselect_b64 s[24:25], -1, 0
	s_and_b64 s[24:25], s[24:25], exec
	s_cselect_b32 s35, s23, s60
	s_cselect_b32 s34, s22, s59
	s_cselect_b32 s30, 0, s61
	s_cselect_b32 s31, s56, s57
	s_lshl_b32 s24, s30, 6
	s_lshl_b32 s62, s31, 14
	s_and_b32 s68, s24, 0x180
	s_or_b32 s24, s68, s62
	s_ashr_i32 s25, s24, 31
	s_lshl_b64 s[26:27], s[24:25], 1
	s_add_u32 s28, s8, s26
	s_addc_u32 s29, s9, s27
	s_lshl_b32 s25, s31, 6
	s_lshr_b32 s26, s30, 3
	ds_read_b128 v[180:183], v174
	ds_read_b128 v[184:187], v174 offset:1024
	ds_read_b128 v[188:191], v174 offset:2048
	ds_read_b128 v[192:195], v174 offset:3072
	ds_read_b128 v[196:199], v174 offset:4096
	ds_read_b128 v[200:203], v174 offset:5120
	ds_read_b128 v[204:207], v174 offset:6144
	ds_read_b128 v[208:211], v174 offset:7168
	s_waitcnt vmcnt(0)
	s_add_i32 s25, s25, s26
	v_pk_add_f16 v8, v8, v12
	v_pk_add_f16 v9, v9, v13
	v_pk_add_f16 v10, v10, v14
	v_pk_add_f16 v11, v11, v15
	s_lshl_b32 s63, s25, 9
	v_pk_max_f16 v11, v11, 0
	v_pk_max_f16 v10, v10, 0
	v_pk_max_f16 v9, v9, 0
	v_pk_max_f16 v8, v8, 0
	v_pk_add_f16 v0, v0, v4
	v_pk_add_f16 v1, v1, v5
	v_pk_add_f16 v2, v2, v6
	v_pk_add_f16 v3, v3, v7
	s_or_b32 s26, s63, s68
	v_pk_max_f16 v3, v3, 0
	v_pk_max_f16 v2, v2, 0
	v_pk_max_f16 v1, v1, 0
	v_pk_max_f16 v0, v0, 0
	ds_write_b128 v175, v[8:11] offset:49152
	ds_write_b128 v175, v[0:3] offset:57344
	s_ashr_i32 s27, s26, 31
	s_lshl_b64 s[30:31], s[26:27], 1
	s_nop 4
	global_load_dwordx4 v[0:3], v168, s[28:29]
	s_add_u32 s30, s10, s30
	global_load_dwordx4 v[4:7], v170, s[28:29]
	s_addc_u32 s31, s11, s31
	global_load_dwordx4 v[8:11], v169, s[30:31]
	global_load_dwordx4 v[12:15], v171, s[30:31]
	s_waitcnt lgkmcnt(2)
	s_barrier
	s_waitcnt lgkmcnt(0)
	s_setprio 1
	s_waitcnt lgkmcnt(0)
	v_mfma_f32_16x16x32_f16 v[136:139], v[144:147], v[180:183], v[136:139]
	v_mfma_f32_16x16x32_f16 v[140:143], v[152:155], v[180:183], v[140:143]
	v_mfma_f32_16x16x32_f16 v[124:127], v[144:147], v[188:191], v[124:127]
	v_mfma_f32_16x16x32_f16 v[120:123], v[152:155], v[188:191], v[120:123]
	v_mfma_f32_16x16x32_f16 v[108:111], v[144:147], v[196:199], v[108:111]
	v_mfma_f32_16x16x32_f16 v[104:107], v[152:155], v[196:199], v[104:107]
	v_mfma_f32_16x16x32_f16 v[92:95], v[144:147], v[204:207], v[92:95]
	v_mfma_f32_16x16x32_f16 v[88:91], v[152:155], v[204:207], v[88:91]
	v_mfma_f32_16x16x32_f16 v[136:139], v[148:151], v[184:187], v[136:139]
	v_mfma_f32_16x16x32_f16 v[140:143], v[156:159], v[184:187], v[140:143]
	v_mfma_f32_16x16x32_f16 v[124:127], v[148:151], v[192:195], v[124:127]
	v_mfma_f32_16x16x32_f16 v[120:123], v[156:159], v[192:195], v[120:123]
	v_mfma_f32_16x16x32_f16 v[108:111], v[148:151], v[200:203], v[108:111]
	v_mfma_f32_16x16x32_f16 v[104:107], v[156:159], v[200:203], v[104:107]
	v_mfma_f32_16x16x32_f16 v[92:95], v[148:151], v[208:211], v[92:95]
	v_mfma_f32_16x16x32_f16 v[88:91], v[156:159], v[208:211], v[88:91]
	s_setprio 0
	s_waitcnt lgkmcnt(0)
	s_setprio 1
	s_waitcnt lgkmcnt(0)
	v_mfma_f32_16x16x32_f16 v[132:135], v[212:215], v[180:183], v[132:135]
	v_mfma_f32_16x16x32_f16 v[128:131], v[220:223], v[180:183], v[128:131]
	v_mfma_f32_16x16x32_f16 v[116:119], v[212:215], v[188:191], v[116:119]
	v_mfma_f32_16x16x32_f16 v[112:115], v[220:223], v[188:191], v[112:115]
	v_mfma_f32_16x16x32_f16 v[100:103], v[212:215], v[196:199], v[100:103]
	v_mfma_f32_16x16x32_f16 v[96:99], v[220:223], v[196:199], v[96:99]
	v_mfma_f32_16x16x32_f16 v[84:87], v[212:215], v[204:207], v[84:87]
	v_mfma_f32_16x16x32_f16 v[80:83], v[220:223], v[204:207], v[80:83]
	v_mfma_f32_16x16x32_f16 v[132:135], v[216:219], v[184:187], v[132:135]
	v_mfma_f32_16x16x32_f16 v[128:131], v[224:227], v[184:187], v[128:131]
	v_mfma_f32_16x16x32_f16 v[116:119], v[216:219], v[192:195], v[116:119]
	v_mfma_f32_16x16x32_f16 v[112:115], v[224:227], v[192:195], v[112:115]
	v_mfma_f32_16x16x32_f16 v[100:103], v[216:219], v[200:203], v[100:103]
	v_mfma_f32_16x16x32_f16 v[96:99], v[224:227], v[200:203], v[96:99]
	v_mfma_f32_16x16x32_f16 v[84:87], v[216:219], v[208:211], v[84:87]
	v_mfma_f32_16x16x32_f16 v[80:83], v[224:227], v[208:211], v[80:83]
	s_setprio 0
	s_or_b32 s64, s62, 0x2000
	s_or_b32 s28, s68, s64
	s_ashr_i32 s29, s28, 31
	s_barrier
	s_add_i32 s81, s51, s44
	v_lshl_add_u64 v[166:167], s[34:35], 0, v[160:161]
	s_mov_b32 m0, s81
	global_load_lds_dwordx4 v[166:167], off
	v_lshl_add_u64 v[228:229], s[34:35], 0, v[162:163]
	s_add_i32 m0, s81, 0x2000
	s_nop 0
	global_load_lds_dwordx4 v[228:229], off
	s_add_u32 s34, s34, s14
	s_addc_u32 s35, s35, s15
	s_add_i32 s82, s52, s44
	v_lshl_add_u64 v[230:231], s[34:35], 0, v[160:161]
	s_mov_b32 m0, s82
	v_lshl_add_u64 v[232:233], s[34:35], 0, v[162:163]
	global_load_lds_dwordx4 v[230:231], off
	s_add_i32 m0, s82, 0x2000
	s_nop 0
	global_load_lds_dwordx4 v[232:233], off
	ds_read_b128 v[180:183], v174 offset:16384
	ds_read_b128 v[184:187], v174 offset:17408
	ds_read_b128 v[188:191], v174 offset:18432
	ds_read_b128 v[192:195], v174 offset:19456
	ds_read_b128 v[196:199], v174 offset:20480
	ds_read_b128 v[200:203], v174 offset:21504
	ds_read_b128 v[204:207], v174 offset:22528
	ds_read_b128 v[208:211], v174 offset:23552
	s_lshl_b64 s[30:31], s[28:29], 1
	s_waitcnt vmcnt(4)
	s_add_u32 s66, s8, s30
	v_pk_add_f16 v0, v0, v8
	v_pk_add_f16 v1, v1, v9
	v_pk_add_f16 v2, v2, v10
	v_pk_add_f16 v3, v3, v11
	s_addc_u32 s67, s9, s31
	s_add_i32 s65, s63, 0x4000
	v_pk_max_f16 v3, v3, 0
	v_pk_max_f16 v2, v2, 0
	v_pk_max_f16 v1, v1, 0
	v_pk_max_f16 v0, v0, 0
	v_pk_add_f16 v4, v4, v12
	v_pk_add_f16 v5, v5, v13
	v_pk_add_f16 v6, v6, v14
	v_pk_add_f16 v7, v7, v15
	s_or_b32 s30, s65, s68
	v_pk_max_f16 v7, v7, 0
	v_pk_max_f16 v6, v6, 0
	v_pk_max_f16 v5, v5, 0
	v_pk_max_f16 v4, v4, 0
	ds_write_b128 v175, v[0:3]
	ds_write_b128 v175, v[4:7] offset:8192
	s_ashr_i32 s31, s30, 31
	s_lshl_b64 s[68:69], s[30:31], 1
	s_nop 4
	global_load_dwordx4 v[0:3], v168, s[66:67]
	s_add_u32 s68, s10, s68
	global_load_dwordx4 v[4:7], v170, s[66:67]
	s_addc_u32 s69, s11, s69
	global_load_dwordx4 v[8:11], v169, s[68:69]
	global_load_dwordx4 v[12:15], v171, s[68:69]
	s_waitcnt lgkmcnt(2)
	s_barrier
	s_waitcnt lgkmcnt(0)
	s_setprio 1
	s_waitcnt lgkmcnt(0)
	v_mfma_f32_16x16x32_f16 v[76:79], v[144:147], v[180:183], v[76:79]
	v_mfma_f32_16x16x32_f16 v[72:75], v[152:155], v[180:183], v[72:75]
	v_mfma_f32_16x16x32_f16 v[60:63], v[144:147], v[188:191], v[60:63]
	v_mfma_f32_16x16x32_f16 v[56:59], v[152:155], v[188:191], v[56:59]
	v_mfma_f32_16x16x32_f16 v[44:47], v[144:147], v[196:199], v[44:47]
	v_mfma_f32_16x16x32_f16 v[40:43], v[152:155], v[196:199], v[40:43]
	v_mfma_f32_16x16x32_f16 v[28:31], v[144:147], v[204:207], v[28:31]
	v_mfma_f32_16x16x32_f16 v[24:27], v[152:155], v[204:207], v[24:27]
	v_mfma_f32_16x16x32_f16 v[76:79], v[148:151], v[184:187], v[76:79]
	v_mfma_f32_16x16x32_f16 v[72:75], v[156:159], v[184:187], v[72:75]
	v_mfma_f32_16x16x32_f16 v[60:63], v[148:151], v[192:195], v[60:63]
	v_mfma_f32_16x16x32_f16 v[56:59], v[156:159], v[192:195], v[56:59]
	v_mfma_f32_16x16x32_f16 v[44:47], v[148:151], v[200:203], v[44:47]
	v_mfma_f32_16x16x32_f16 v[40:43], v[156:159], v[200:203], v[40:43]
	v_mfma_f32_16x16x32_f16 v[28:31], v[148:151], v[208:211], v[28:31]
	v_mfma_f32_16x16x32_f16 v[24:27], v[156:159], v[208:211], v[24:27]
	s_setprio 0
	s_setprio 1
	v_mfma_f32_16x16x32_f16 v[68:71], v[212:215], v[180:183], v[68:71]
	v_mfma_f32_16x16x32_f16 v[64:67], v[220:223], v[180:183], v[64:67]
	v_mfma_f32_16x16x32_f16 v[52:55], v[212:215], v[188:191], v[52:55]
	v_mfma_f32_16x16x32_f16 v[48:51], v[220:223], v[188:191], v[48:51]
	v_mfma_f32_16x16x32_f16 v[36:39], v[212:215], v[196:199], v[36:39]
	v_mfma_f32_16x16x32_f16 v[32:35], v[220:223], v[196:199], v[32:35]
	v_mfma_f32_16x16x32_f16 v[20:23], v[212:215], v[204:207], v[20:23]
	v_mfma_f32_16x16x32_f16 v[16:19], v[220:223], v[204:207], v[16:19]
	v_mfma_f32_16x16x32_f16 v[68:71], v[216:219], v[184:187], v[68:71]
	v_mfma_f32_16x16x32_f16 v[64:67], v[224:227], v[184:187], v[64:67]
	v_mfma_f32_16x16x32_f16 v[52:55], v[216:219], v[192:195], v[52:55]
	v_mfma_f32_16x16x32_f16 v[48:51], v[224:227], v[192:195], v[48:51]
	v_mfma_f32_16x16x32_f16 v[36:39], v[216:219], v[200:203], v[36:39]
	v_mfma_f32_16x16x32_f16 v[32:35], v[224:227], v[200:203], v[32:35]
	v_mfma_f32_16x16x32_f16 v[20:23], v[216:219], v[208:211], v[20:23]
	v_mfma_f32_16x16x32_f16 v[16:19], v[224:227], v[208:211], v[16:19]
	s_setprio 0
	s_barrier
	ds_read_b128 v[144:147], v178
	ds_read_b128 v[148:151], v178 offset:1024
	ds_read_b128 v[152:155], v178 offset:2048
	ds_read_b128 v[156:159], v178 offset:3072
	ds_read_b128 v[212:215], v179
	ds_read_b128 v[216:219], v179 offset:1024
	ds_read_b128 v[220:223], v179 offset:2048
	ds_read_b128 v[224:227], v179 offset:3072
	s_ashr_i32 s25, s62, 31
	s_lshl_b64 s[24:25], s[24:25], 1
	s_add_u32 s24, s8, s24
	s_addc_u32 s25, s9, s25
	ds_read_b128 v[180:183], v174 offset:32768
	ds_read_b128 v[184:187], v174 offset:33792
	ds_read_b128 v[188:191], v174 offset:34816
	ds_read_b128 v[192:195], v174 offset:35840
	ds_read_b128 v[196:199], v174 offset:36864
	ds_read_b128 v[200:203], v174 offset:37888
	ds_read_b128 v[204:207], v174 offset:38912
	ds_read_b128 v[208:211], v174 offset:39936
	s_waitcnt vmcnt(0)
	s_add_u32 s24, s24, 0x80
	v_pk_add_f16 v0, v0, v8
	v_pk_add_f16 v1, v1, v9
	v_pk_add_f16 v2, v2, v10
	v_pk_add_f16 v3, v3, v11
	s_addc_u32 s25, s25, 0
	s_ashr_i32 s27, s63, 31
	v_pk_max_f16 v3, v3, 0
	v_pk_max_f16 v2, v2, 0
	v_pk_max_f16 v1, v1, 0
	v_pk_max_f16 v0, v0, 0
	v_pk_add_f16 v4, v4, v12
	v_pk_add_f16 v5, v5, v13
	v_pk_add_f16 v6, v6, v14
	v_pk_add_f16 v7, v7, v15
	s_lshl_b64 s[26:27], s[26:27], 1
	v_pk_max_f16 v7, v7, 0
	v_pk_max_f16 v6, v6, 0
	v_pk_max_f16 v5, v5, 0
	v_pk_max_f16 v4, v4, 0
	ds_write_b128 v175, v[0:3] offset:16384
	ds_write_b128 v175, v[4:7] offset:24576
	s_add_u32 s26, s10, s26
	s_addc_u32 s27, s11, s27
	s_nop 4
	global_load_dwordx4 v[0:3], v168, s[24:25]
	s_add_u32 s26, s26, 0x80
	global_load_dwordx4 v[4:7], v170, s[24:25]
	s_addc_u32 s27, s27, 0
	global_load_dwordx4 v[8:11], v169, s[26:27]
	global_load_dwordx4 v[12:15], v171, s[26:27]
	s_waitcnt lgkmcnt(2)
	s_barrier
	s_waitcnt lgkmcnt(0)
	s_setprio 1
	s_waitcnt lgkmcnt(0)
	v_mfma_f32_16x16x32_f16 v[136:139], v[144:147], v[180:183], v[136:139]
	v_mfma_f32_16x16x32_f16 v[140:143], v[152:155], v[180:183], v[140:143]
	v_mfma_f32_16x16x32_f16 v[124:127], v[144:147], v[188:191], v[124:127]
	v_mfma_f32_16x16x32_f16 v[120:123], v[152:155], v[188:191], v[120:123]
	v_mfma_f32_16x16x32_f16 v[108:111], v[144:147], v[196:199], v[108:111]
	v_mfma_f32_16x16x32_f16 v[104:107], v[152:155], v[196:199], v[104:107]
	v_mfma_f32_16x16x32_f16 v[92:95], v[144:147], v[204:207], v[92:95]
	v_mfma_f32_16x16x32_f16 v[88:91], v[152:155], v[204:207], v[88:91]
	v_mfma_f32_16x16x32_f16 v[136:139], v[148:151], v[184:187], v[136:139]
	v_mfma_f32_16x16x32_f16 v[140:143], v[156:159], v[184:187], v[140:143]
	v_mfma_f32_16x16x32_f16 v[124:127], v[148:151], v[192:195], v[124:127]
	v_mfma_f32_16x16x32_f16 v[120:123], v[156:159], v[192:195], v[120:123]
	v_mfma_f32_16x16x32_f16 v[108:111], v[148:151], v[200:203], v[108:111]
	v_mfma_f32_16x16x32_f16 v[104:107], v[156:159], v[200:203], v[104:107]
	v_mfma_f32_16x16x32_f16 v[92:95], v[148:151], v[208:211], v[92:95]
	v_mfma_f32_16x16x32_f16 v[88:91], v[156:159], v[208:211], v[88:91]
	s_setprio 0
	s_waitcnt lgkmcnt(0)
	s_setprio 1
	s_waitcnt lgkmcnt(0)
	v_mfma_f32_16x16x32_f16 v[132:135], v[212:215], v[180:183], v[132:135]
	v_mfma_f32_16x16x32_f16 v[128:131], v[220:223], v[180:183], v[128:131]
	v_mfma_f32_16x16x32_f16 v[116:119], v[212:215], v[188:191], v[116:119]
	v_mfma_f32_16x16x32_f16 v[112:115], v[220:223], v[188:191], v[112:115]
	v_mfma_f32_16x16x32_f16 v[100:103], v[212:215], v[196:199], v[100:103]
	v_mfma_f32_16x16x32_f16 v[96:99], v[220:223], v[196:199], v[96:99]
	v_mfma_f32_16x16x32_f16 v[84:87], v[212:215], v[204:207], v[84:87]
	v_mfma_f32_16x16x32_f16 v[80:83], v[220:223], v[204:207], v[80:83]
	v_mfma_f32_16x16x32_f16 v[132:135], v[216:219], v[184:187], v[132:135]
	v_mfma_f32_16x16x32_f16 v[128:131], v[224:227], v[184:187], v[128:131]
	v_mfma_f32_16x16x32_f16 v[116:119], v[216:219], v[192:195], v[116:119]
	v_mfma_f32_16x16x32_f16 v[112:115], v[224:227], v[192:195], v[112:115]
	v_mfma_f32_16x16x32_f16 v[100:103], v[216:219], v[200:203], v[100:103]
	v_mfma_f32_16x16x32_f16 v[96:99], v[224:227], v[200:203], v[96:99]
	v_mfma_f32_16x16x32_f16 v[84:87], v[216:219], v[208:211], v[84:87]
	v_mfma_f32_16x16x32_f16 v[80:83], v[224:227], v[208:211], v[80:83]
	s_setprio 0
	s_ashr_i32 s29, s64, 31
	s_lshl_b64 s[24:25], s[28:29], 1
	s_add_u32 s24, s8, s24
	s_barrier
	s_add_i32 s81, s53, s44
	v_lshl_add_u64 v[166:167], v[166:167], 0, s[20:21]
	s_mov_b32 m0, s81
	global_load_lds_dwordx4 v[166:167], off
	v_lshl_add_u64 v[166:167], v[228:229], 0, s[20:21]
	s_add_i32 m0, s81, 0x2000
	s_nop 0
	global_load_lds_dwordx4 v[166:167], off
	s_add_i32 s82, s54, s44
	v_lshl_add_u64 v[248:249], v[230:231], 0, s[20:21]
	s_mov_b32 m0, s82
	s_nop 0
	global_load_lds_dwordx4 v[248:249], off
	v_lshl_add_u64 v[248:249], v[232:233], 0, s[20:21]
	s_add_i32 m0, s82, 0x2000
	s_nop 0
	global_load_lds_dwordx4 v[248:249], off
	ds_read_b128 v[180:183], v174 offset:49152
	ds_read_b128 v[184:187], v174 offset:50176
	ds_read_b128 v[188:191], v174 offset:51200
	ds_read_b128 v[192:195], v174 offset:52224
	ds_read_b128 v[196:199], v174 offset:53248
	ds_read_b128 v[200:203], v174 offset:54272
	ds_read_b128 v[204:207], v174 offset:55296
	ds_read_b128 v[208:211], v174 offset:56320
	s_addc_u32 s25, s9, s25
	s_waitcnt vmcnt(4)
	s_add_u32 s24, s24, 0x80
	v_pk_add_f16 v0, v0, v8
	v_pk_add_f16 v1, v1, v9
	v_pk_add_f16 v2, v2, v10
	v_pk_add_f16 v3, v3, v11
	s_addc_u32 s25, s25, 0
	s_ashr_i32 s31, s65, 31
	v_pk_max_f16 v3, v3, 0
	v_pk_max_f16 v2, v2, 0
	v_pk_max_f16 v1, v1, 0
	v_pk_max_f16 v0, v0, 0
	v_pk_add_f16 v4, v4, v12
	v_pk_add_f16 v5, v5, v13
	v_pk_add_f16 v6, v6, v14
	v_pk_add_f16 v7, v7, v15
	s_lshl_b64 s[26:27], s[30:31], 1
	v_pk_max_f16 v7, v7, 0
	v_pk_max_f16 v6, v6, 0
	v_pk_max_f16 v5, v5, 0
	v_pk_max_f16 v4, v4, 0
	ds_write_b128 v175, v[0:3] offset:32768
	ds_write_b128 v175, v[4:7] offset:40960
	s_add_u32 s26, s10, s26
	s_addc_u32 s27, s11, s27
	s_nop 4
	global_load_dwordx4 v[8:11], v168, s[24:25]
	s_add_u32 s26, s26, 0x80
	global_load_dwordx4 v[0:3], v170, s[24:25]
	s_addc_u32 s27, s27, 0
	global_load_dwordx4 v[12:15], v169, s[26:27]
	global_load_dwordx4 v[4:7], v171, s[26:27]
	s_waitcnt lgkmcnt(2)
	s_barrier
	s_waitcnt lgkmcnt(0)
	s_setprio 1
	s_waitcnt lgkmcnt(0)
	v_mfma_f32_16x16x32_f16 v[76:79], v[144:147], v[180:183], v[76:79]
	v_mfma_f32_16x16x32_f16 v[72:75], v[152:155], v[180:183], v[72:75]
	v_mfma_f32_16x16x32_f16 v[60:63], v[144:147], v[188:191], v[60:63]
	v_mfma_f32_16x16x32_f16 v[56:59], v[152:155], v[188:191], v[56:59]
	v_mfma_f32_16x16x32_f16 v[44:47], v[144:147], v[196:199], v[44:47]
	v_mfma_f32_16x16x32_f16 v[40:43], v[152:155], v[196:199], v[40:43]
	v_mfma_f32_16x16x32_f16 v[28:31], v[144:147], v[204:207], v[28:31]
	v_mfma_f32_16x16x32_f16 v[24:27], v[152:155], v[204:207], v[24:27]
	v_mfma_f32_16x16x32_f16 v[76:79], v[148:151], v[184:187], v[76:79]
	v_mfma_f32_16x16x32_f16 v[72:75], v[156:159], v[184:187], v[72:75]
	v_mfma_f32_16x16x32_f16 v[60:63], v[148:151], v[192:195], v[60:63]
	v_mfma_f32_16x16x32_f16 v[56:59], v[156:159], v[192:195], v[56:59]
	v_mfma_f32_16x16x32_f16 v[44:47], v[148:151], v[200:203], v[44:47]
	v_mfma_f32_16x16x32_f16 v[40:43], v[156:159], v[200:203], v[40:43]
	v_mfma_f32_16x16x32_f16 v[28:31], v[148:151], v[208:211], v[28:31]
	v_mfma_f32_16x16x32_f16 v[24:27], v[156:159], v[208:211], v[24:27]
	s_setprio 0
	s_setprio 1
	v_mfma_f32_16x16x32_f16 v[68:71], v[212:215], v[180:183], v[68:71]
	v_mfma_f32_16x16x32_f16 v[64:67], v[220:223], v[180:183], v[64:67]
	v_mfma_f32_16x16x32_f16 v[52:55], v[212:215], v[188:191], v[52:55]
	v_mfma_f32_16x16x32_f16 v[48:51], v[220:223], v[188:191], v[48:51]
	v_mfma_f32_16x16x32_f16 v[36:39], v[212:215], v[196:199], v[36:39]
	v_mfma_f32_16x16x32_f16 v[32:35], v[220:223], v[196:199], v[32:35]
	v_mfma_f32_16x16x32_f16 v[20:23], v[212:215], v[204:207], v[20:23]
	v_mfma_f32_16x16x32_f16 v[16:19], v[220:223], v[204:207], v[16:19]
	v_mfma_f32_16x16x32_f16 v[68:71], v[216:219], v[184:187], v[68:71]
	v_mfma_f32_16x16x32_f16 v[64:67], v[224:227], v[184:187], v[64:67]
	v_mfma_f32_16x16x32_f16 v[52:55], v[216:219], v[192:195], v[52:55]
	v_mfma_f32_16x16x32_f16 v[48:51], v[224:227], v[192:195], v[48:51]
	v_mfma_f32_16x16x32_f16 v[36:39], v[216:219], v[200:203], v[36:39]
	v_mfma_f32_16x16x32_f16 v[32:35], v[224:227], v[200:203], v[32:35]
	v_mfma_f32_16x16x32_f16 v[20:23], v[216:219], v[208:211], v[20:23]
	v_mfma_f32_16x16x32_f16 v[16:19], v[224:227], v[208:211], v[16:19]
	s_setprio 0
	s_add_i32 s24, s61, 2
	s_add_u32 s59, s59, 0x100
	s_addc_u32 s60, s60, 0
	s_cmp_ge_i32 s61, s49
	s_mov_b32 s61, s24
	s_barrier
	s_cbranch_scc0 .LBB8_37
	s_branch .LBB8_45

	.amdhsa_kernel _Z14k_phase_gen_utIN3pg86EpiH16ILb0ELb1EEENS1_ILb1ELb0EEEEvNS0_4GemmES4_NS0_6GenSrcET_T0_
		.amdhsa_group_segment_fixed_size 0
		.amdhsa_private_segment_fixed_size 0
		.amdhsa_kernarg_size 384
		.amdhsa_user_sgpr_count 2
		.amdhsa_user_sgpr_dispatch_ptr 0
		.amdhsa_user_sgpr_queue_ptr 0
		.amdhsa_user_sgpr_kernarg_segment_ptr 1
		.amdhsa_user_sgpr_dispatch_id 0
		.amdhsa_user_sgpr_kernarg_preload_length 0
		.amdhsa_user_sgpr_kernarg_preload_offset 0
		.amdhsa_user_sgpr_private_segment_size 0
		.amdhsa_uses_dynamic_stack 0
		.amdhsa_enable_private_segment 0
		.amdhsa_system_sgpr_workgroup_id_x 1
		.amdhsa_system_sgpr_workgroup_id_y 0
		.amdhsa_system_sgpr_workgroup_id_z 0
		.amdhsa_system_sgpr_workgroup_info 0
		.amdhsa_system_vgpr_workitem_id 0
		.amdhsa_next_free_vgpr 252
		.amdhsa_next_free_sgpr 83
		.amdhsa_accum_offset 252
		.amdhsa_reserve_vcc 1
		.amdhsa_float_round_mode_32 0
		.amdhsa_float_round_mode_16_64 0
		.amdhsa_float_denorm_mode_32 3
		.amdhsa_float_denorm_mode_16_64 3
		.amdhsa_dx10_clamp 1
		.amdhsa_ieee_mode 1
		.amdhsa_fp16_overflow 0
		.amdhsa_tg_split 0
		.amdhsa_exception_fp_ieee_invalid_op 0
		.amdhsa_exception_fp_denorm_src 0
		.amdhsa_exception_fp_ieee_div_zero 0
		.amdhsa_exception_fp_ieee_overflow 0
		.amdhsa_exception_fp_ieee_underflow 0
		.amdhsa_exception_fp_ieee_inexact 0
		.amdhsa_exception_int_div_zero 0
	.end_amdhsa_kernel

amdhsa.kernels:
  - .agpr_count:     0
    .args:
      - .offset:         0
        .size:           32
        .value_kind:     by_value
      - .address_space:  global
        .offset:         32
        .size:           8
        .value_kind:     global_buffer
      - .address_space:  global
        .offset:         40
        .size:           8
        .value_kind:     global_buffer
      - .offset:         48
        .size:           4
        .value_kind:     by_value
      - .offset:         56
        .size:           4
        .value_kind:     hidden_block_count_x
      - .offset:         60
        .size:           4
        .value_kind:     hidden_block_count_y
      - .offset:         64
        .size:           4
        .value_kind:     hidden_block_count_z
      - .offset:         68
        .size:           2
        .value_kind:     hidden_group_size_x
      - .offset:         70
        .size:           2
        .value_kind:     hidden_group_size_y
      - .offset:         72
        .size:           2
        .value_kind:     hidden_group_size_z
      - .offset:         74
        .size:           2
        .value_kind:     hidden_remainder_x
      - .offset:         76
        .size:           2
        .value_kind:     hidden_remainder_y
      - .offset:         78
        .size:           2
        .value_kind:     hidden_remainder_z
      - .offset:         96
        .size:           8
        .value_kind:     hidden_global_offset_x
      - .offset:         104
        .size:           8
        .value_kind:     hidden_global_offset_y
      - .offset:         112
        .size:           8
        .value_kind:     hidden_global_offset_z
      - .offset:         120
        .size:           2
        .value_kind:     hidden_grid_dims
      - .offset:         176
        .size:           4
        .value_kind:     hidden_dynamic_lds_size
    .group_segment_fixed_size: 0
    .kernarg_segment_align: 8
    .kernarg_segment_size: 312
    .language:       OpenCL C
    .language_version:
      - 2
      - 0
    .max_flat_workgroup_size: 512
    .name:           _Z10k_phase_hmN3pg84GemmEPDF16_PKfi
    .private_segment_fixed_size: 0
    .sgpr_count:     68
    .sgpr_spill_count: 0
    .symbol:         _Z10k_phase_hmN3pg84GemmEPDF16_PKfi.kd
    .uniform_work_group_size: 1
    .uses_dynamic_stack: false
    .vgpr_count:     140
    .vgpr_spill_count: 0
    .wavefront_size: 64
  - .agpr_count:     0
    .args:
      - .offset:         0
        .size:           32
        .value_kind:     by_value
      - .address_space:  global
        .offset:         32
        .size:           8
        .value_kind:     global_buffer
      - .address_space:  global
        .offset:         40
        .size:           8
        .value_kind:     global_buffer
      - .offset:         48
        .size:           4
        .value_kind:     by_value
      - .offset:         56
        .size:           4
        .value_kind:     hidden_block_count_x
      - .offset:         60
        .size:           4
        .value_kind:     hidden_block_count_y
      - .offset:         64
        .size:           4
        .value_kind:     hidden_block_count_z
      - .offset:         68
        .size:           2
        .value_kind:     hidden_group_size_x
      - .offset:         70
        .size:           2
        .value_kind:     hidden_group_size_y
      - .offset:         72
        .size:           2
        .value_kind:     hidden_group_size_z
      - .offset:         74
        .size:           2
        .value_kind:     hidden_remainder_x
      - .offset:         76
        .size:           2
        .value_kind:     hidden_remainder_y
      - .offset:         78
        .size:           2
        .value_kind:     hidden_remainder_z
      - .offset:         96
        .size:           8
        .value_kind:     hidden_global_offset_x
      - .offset:         104
        .size:           8
        .value_kind:     hidden_global_offset_y
      - .offset:         112
        .size:           8
        .value_kind:     hidden_global_offset_z
      - .offset:         120
        .size:           2
        .value_kind:     hidden_grid_dims
      - .offset:         176
        .size:           4
        .value_kind:     hidden_dynamic_lds_size
    .group_segment_fixed_size: 0
    .kernarg_segment_align: 8
    .kernarg_segment_size: 312
    .language:       OpenCL C
    .language_version:
      - 2
      - 0
    .max_flat_workgroup_size: 512
    .name:           _Z10k_phase_qmN3pg84GemmEPDF16_PKfi
    .private_segment_fixed_size: 0
    .sgpr_count:     67
    .sgpr_spill_count: 0
    .symbol:         _Z10k_phase_qmN3pg84GemmEPDF16_PKfi.kd
    .uniform_work_group_size: 1
    .uses_dynamic_stack: false
    .vgpr_count:     102
    .vgpr_spill_count: 0
    .wavefront_size: 64
  - .agpr_count:     0
    .args:
      - .offset:         0
        .size:           288
        .value_kind:     by_value
    .group_segment_fixed_size: 16640
    .kernarg_segment_align: 8
    .kernarg_segment_size: 288
    .language:       OpenCL C
    .language_version:
      - 2
      - 0
    .max_flat_workgroup_size: 256
    .name:           _Z11prep_kernel8PrepArgs
    .private_segment_fixed_size: 0
    .sgpr_count:     26
    .sgpr_spill_count: 0
    .symbol:         _Z11prep_kernel8PrepArgs.kd
    .uniform_work_group_size: 1
    .uses_dynamic_stack: false
    .vgpr_count:     35
    .vgpr_spill_count: 0
    .wavefront_size: 64
  - .agpr_count:     0
    .args:
      - .actual_access:  read_only
        .address_space:  global
        .offset:         0
        .size:           8
        .value_kind:     global_buffer
      - .actual_access:  read_only
        .address_space:  global
        .offset:         8
        .size:           8
        .value_kind:     global_buffer
      - .actual_access:  read_only
        .address_space:  global
        .offset:         16
        .size:           8
        .value_kind:     global_buffer
      - .actual_access:  write_only
        .address_space:  global
        .offset:         24
        .size:           8
        .value_kind:     global_buffer
    .group_segment_fixed_size: 0
    .kernarg_segment_align: 8
    .kernarg_segment_size: 32
    .language:       OpenCL C
    .language_version:
      - 2
      - 0
    .max_flat_workgroup_size: 256
    .name:           _Z11leaf_kernelPKfS0_PKiPDF16_
    .private_segment_fixed_size: 0
    .sgpr_count:     18
    .sgpr_spill_count: 0
    .symbol:         _Z11leaf_kernelPKfS0_PKiPDF16_.kd
    .uniform_work_group_size: 1
    .uses_dynamic_stack: false
    .vgpr_count:     25
    .vgpr_spill_count: 0
    .wavefront_size: 64
  - .agpr_count:     248
    .args:
      - .actual_access:  read_only
        .address_space:  global
        .offset:         0
        .size:           8
        .value_kind:     global_buffer
      - .actual_access:  read_only
        .address_space:  global
        .offset:         8
        .size:           8
        .value_kind:     global_buffer
      - .actual_access:  write_only
        .address_space:  global
        .offset:         16
        .size:           8
        .value_kind:     global_buffer
      - .actual_access:  write_only
        .address_space:  global
        .offset:         24
        .size:           8
        .value_kind:     global_buffer
    .group_segment_fixed_size: 0
    .kernarg_segment_align: 8
    .kernarg_segment_size: 32
    .language:       OpenCL C
    .language_version:
      - 2
      - 0
    .max_flat_workgroup_size: 256
    .name:           _Z10rnn_kernelPKDF16_S0_PDF16_S1_
    .private_segment_fixed_size: 0
    .sgpr_count:     22
    .sgpr_spill_count: 0
    .symbol:         _Z10rnn_kernelPKDF16_S0_PDF16_S1_.kd
    .uniform_work_group_size: 1
    .uses_dynamic_stack: false
    .vgpr_count:     496
    .vgpr_spill_count: 0
    .wavefront_size: 64
  - .agpr_count:     0
    .args:
      - .actual_access:  read_only
        .address_space:  global
        .offset:         0
        .size:           8
        .value_kind:     global_buffer
      - .actual_access:  read_only
        .address_space:  global
        .offset:         8
        .size:           8
        .value_kind:     global_buffer
      - .actual_access:  write_only
        .address_space:  global
        .offset:         16
        .size:           8
        .value_kind:     global_buffer
    .group_segment_fixed_size: 0
    .kernarg_segment_align: 8
    .kernarg_segment_size: 24
    .language:       OpenCL C
    .language_version:
      - 2
      - 0
    .max_flat_workgroup_size: 256
    .name:           _Z10max_kernelPKDF16_S0_PDF16_
    .private_segment_fixed_size: 0
    .sgpr_count:     18
    .sgpr_spill_count: 0
    .symbol:         _Z10max_kernelPKDF16_S0_PDF16_.kd
    .uniform_work_group_size: 1
    .uses_dynamic_stack: false
    .vgpr_count:     38
    .vgpr_spill_count: 0
    .wavefront_size: 64
  - .agpr_count:     0
    .args:
      - .actual_access:  read_only
        .address_space:  global
        .offset:         0
        .size:           8
        .value_kind:     global_buffer
      - .actual_access:  read_only
        .address_space:  global
        .offset:         8
        .size:           8
        .value_kind:     global_buffer
      - .actual_access:  read_only
        .address_space:  global
        .offset:         16
        .size:           8
        .value_kind:     global_buffer
      - .actual_access:  write_only
        .address_space:  global
        .offset:         24
        .size:           8
        .value_kind:     global_buffer
    .group_segment_fixed_size: 0
    .kernarg_segment_align: 8
    .kernarg_segment_size: 32
    .language:       OpenCL C
    .language_version:
      - 2
      - 0
    .max_flat_workgroup_size: 256
    .name:           _Z12final_kernelPKfS0_S0_Pf
    .private_segment_fixed_size: 0
    .sgpr_count:     14
    .sgpr_spill_count: 0
    .symbol:         _Z12final_kernelPKfS0_S0_Pf.kd
    .uniform_work_group_size: 1
    .uses_dynamic_stack: false
    .vgpr_count:     23
    .vgpr_spill_count: 0
    .wavefront_size: 64
  - .agpr_count:     0
    .args:
      - .address_space:  global
        .offset:         0
        .size:           8
        .value_kind:     global_buffer
      - .offset:         8
        .size:           4
        .value_kind:     by_value
      - .address_space:  global
        .offset:         16
        .size:           8
        .value_kind:     global_buffer
      - .offset:         24
        .size:           4
        .value_kind:     by_value
      - .actual_access:  write_only
        .address_space:  global
        .offset:         32
        .size:           8
        .value_kind:     global_buffer
      - .offset:         40
        .size:           4
        .value_kind:     by_value
      - .actual_access:  read_only
        .address_space:  global
        .offset:         48
        .size:           8
        .value_kind:     global_buffer
    .group_segment_fixed_size: 0
    .kernarg_segment_align: 8
    .kernarg_segment_size: 56
    .language:       OpenCL C
    .language_version:
      - 2
      - 0
    .max_flat_workgroup_size: 512
    .name:           _Z9tg_kernelILi64ELi8ELi3ELb0EEvPKDF16_iS1_iPviPKf
    .private_segment_fixed_size: 0
    .sgpr_count:     26
    .sgpr_spill_count: 0
    .symbol:         _Z9tg_kernelILi64ELi8ELi3ELb0EEvPKDF16_iS1_iPviPKf.kd
    .uniform_work_group_size: 1
    .uses_dynamic_stack: false
    .vgpr_count:     62
    .vgpr_spill_count: 0
    .wavefront_size: 64
  - .agpr_count:     0
    .args:
      - .offset:         0
        .size:           32
        .value_kind:     by_value
      - .offset:         32
        .size:           32
        .value_kind:     by_value
      - .offset:         64
        .size:           16
        .value_kind:     by_value
      - .offset:         80
        .size:           24
        .value_kind:     by_value
      - .offset:         104
        .size:           24
        .value_kind:     by_value
      - .offset:         128
        .size:           4
        .value_kind:     hidden_block_count_x
      - .offset:         132
        .size:           4
        .value_kind:     hidden_block_count_y
      - .offset:         136
        .size:           4
        .value_kind:     hidden_block_count_z
      - .offset:         140
        .size:           2
        .value_kind:     hidden_group_size_x
      - .offset:         142
        .size:           2
        .value_kind:     hidden_group_size_y
      - .offset:         144
        .size:           2
        .value_kind:     hidden_group_size_z
      - .offset:         146
        .size:           2
        .value_kind:     hidden_remainder_x
      - .offset:         148
        .size:           2
        .value_kind:     hidden_remainder_y
      - .offset:         150
        .size:           2
        .value_kind:     hidden_remainder_z
      - .offset:         168
        .size:           8
        .value_kind:     hidden_global_offset_x
      - .offset:         176
        .size:           8
        .value_kind:     hidden_global_offset_y
      - .offset:         184
        .size:           8
        .value_kind:     hidden_global_offset_z
      - .offset:         192
        .size:           2
        .value_kind:     hidden_grid_dims
      - .offset:         248
        .size:           4
        .value_kind:     hidden_dynamic_lds_size
    .group_segment_fixed_size: 0
    .kernarg_segment_align: 8
    .kernarg_segment_size: 384
    .language:       OpenCL C
    .language_version:
      - 2
      - 0
    .max_flat_workgroup_size: 512
    .name:           _Z14k_phase_gen_utIN3pg86EpiH16ILb0ELb1EEENS1_ILb1ELb0EEEEvNS0_4GemmES4_NS0_6GenSrcET_T0_
    .private_segment_fixed_size: 0
    .sgpr_count:     89
    .sgpr_spill_count: 0
    .symbol:         _Z14k_phase_gen_utIN3pg86EpiH16ILb0ELb1EEENS1_ILb1ELb0EEEEvNS0_4GemmES4_NS0_6GenSrcET_T0_.kd
    .uniform_work_group_size: 1
    .uses_dynamic_stack: false
    .vgpr_count:     252
    .vgpr_spill_count: 0
    .wavefront_size: 64
  - .agpr_count:     0
    .args:
      - .address_space:  global
        .offset:         0
        .size:           8
        .value_kind:     global_buffer
      - .offset:         8
        .size:           4
        .value_kind:     by_value
      - .address_space:  global
        .offset:         16
        .size:           8
        .value_kind:     global_buffer
      - .offset:         24
        .size:           4
        .value_kind:     by_value
      - .actual_access:  write_only
        .address_space:  global
        .offset:         32
        .size:           8
        .value_kind:     global_buffer
      - .offset:         40
        .size:           4
        .value_kind:     by_value
      - .actual_access:  read_only
        .address_space:  global
        .offset:         48
        .size:           8
        .value_kind:     global_buffer
      - .offset:         56
        .size:           4
        .value_kind:     hidden_block_count_x
      - .offset:         60
        .size:           4
        .value_kind:     hidden_block_count_y
      - .offset:         64
        .size:           4
        .value_kind:     hidden_block_count_z
      - .offset:         68
        .size:           2
        .value_kind:     hidden_group_size_x
      - .offset:         70
        .size:           2
        .value_kind:     hidden_group_size_y
      - .offset:         72
        .size:           2
        .value_kind:     hidden_group_size_z
      - .offset:         74
        .size:           2
        .value_kind:     hidden_remainder_x
      - .offset:         76
        .size:           2
        .value_kind:     hidden_remainder_y
      - .offset:         78
        .size:           2
        .value_kind:     hidden_remainder_z
      - .offset:         96
        .size:           8
        .value_kind:     hidden_global_offset_x
      - .offset:         104
        .size:           8
        .value_kind:     hidden_global_offset_y
      - .offset:         112
        .size:           8
        .value_kind:     hidden_global_offset_z
      - .offset:         120
        .size:           2
        .value_kind:     hidden_grid_dims
      - .offset:         176
        .size:           4
        .value_kind:     hidden_dynamic_lds_size
    .group_segment_fixed_size: 0
    .kernarg_segment_align: 8
    .kernarg_segment_size: 312
    .language:       OpenCL C
    .language_version:
      - 2
      - 0
    .max_flat_workgroup_size: 512
    .name:           _Z9tg_kernelILi128ELi8ELi1ELb1EEvPKDF16_iS1_iPviPKf
    .private_segment_fixed_size: 0
    .sgpr_count:     25
    .sgpr_spill_count: 0
    .symbol:         _Z9tg_kernelILi128ELi8ELi1ELb1EEvPKDF16_iS1_iPviPKf.kd
    .uniform_work_group_size: 1
    .uses_dynamic_stack: false
    .vgpr_count:     96
    .vgpr_spill_count: 0
    .wavefront_size: 64
  - .agpr_count:     0
    .args:
      - .address_space:  global
        .offset:         0
        .size:           8
        .value_kind:     global_buffer
      - .offset:         8
        .size:           4
        .value_kind:     by_value
      - .address_space:  global
        .offset:         16
        .size:           8
        .value_kind:     global_buffer
      - .offset:         24
        .size:           4
        .value_kind:     by_value
      - .actual_access:  write_only
        .address_space:  global
        .offset:         32
        .size:           8
        .value_kind:     global_buffer
      - .offset:         40
        .size:           4
        .value_kind:     by_value
      - .actual_access:  read_only
        .address_space:  global
        .offset:         48
        .size:           8
        .value_kind:     global_buffer
    .group_segment_fixed_size: 0
    .kernarg_segment_align: 8
    .kernarg_segment_size: 56
    .language:       OpenCL C
    .language_version:
      - 2
      - 0
    .max_flat_workgroup_size: 512
    .name:           _Z9tg_kernelILi64ELi8ELi1ELb0EEvPKDF16_iS1_iPviPKf
    .private_segment_fixed_size: 0
    .sgpr_count:     26
    .sgpr_spill_count: 0
    .symbol:         _Z9tg_kernelILi64ELi8ELi1ELb0EEvPKDF16_iS1_iPviPKf.kd
    .uniform_work_group_size: 1
    .uses_dynamic_stack: false
    .vgpr_count:     62
    .vgpr_spill_count: 0
    .wavefront_size: 64
  - .agpr_count:     0
    .args:
      - .address_space:  global
        .offset:         0
        .size:           8
        .value_kind:     global_buffer
      - .offset:         8
        .size:           4
        .value_kind:     by_value
      - .address_space:  global
        .offset:         16
        .size:           8
        .value_kind:     global_buffer
      - .offset:         24
        .size:           4
        .value_kind:     by_value
      - .actual_access:  write_only
        .address_space:  global
        .offset:         32
        .size:           8
        .value_kind:     global_buffer
      - .offset:         40
        .size:           4
        .value_kind:     by_value
      - .actual_access:  read_only
        .address_space:  global
        .offset:         48
        .size:           8
        .value_kind:     global_buffer
    .group_segment_fixed_size: 0
    .kernarg_segment_align: 8
    .kernarg_segment_size: 56
    .language:       OpenCL C
    .language_version:
      - 2
      - 0
    .max_flat_workgroup_size: 512
    .name:           _Z9tg_kernelILi64ELi8ELi4ELb0EEvPKDF16_iS1_iPviPKf
    .private_segment_fixed_size: 0
    .sgpr_count:     26
    .sgpr_spill_count: 0
    .symbol:         _Z9tg_kernelILi64ELi8ELi4ELb0EEvPKDF16_iS1_iPviPKf.kd
    .uniform_work_group_size: 1
    .uses_dynamic_stack: false
    .vgpr_count:     64
    .vgpr_spill_count: 0
    .wavefront_size: 64
  - .agpr_count:     0
    .args:
      - .address_space:  global
        .offset:         0
        .size:           8
        .value_kind:     global_buffer
      - .offset:         8
        .size:           4
        .value_kind:     by_value
      - .address_space:  global
        .offset:         16
        .size:           8
        .value_kind:     global_buffer
      - .offset:         24
        .size:           4
        .value_kind:     by_value
      - .actual_access:  write_only
        .address_space:  global
        .offset:         32
        .size:           8
        .value_kind:     global_buffer
      - .offset:         40
        .size:           4
        .value_kind:     by_value
      - .actual_access:  read_only
        .address_space:  global
        .offset:         48
        .size:           8
        .value_kind:     global_buffer
    .group_segment_fixed_size: 0
    .kernarg_segment_align: 8
    .kernarg_segment_size: 56
    .language:       OpenCL C
    .language_version:
      - 2
      - 0
    .max_flat_workgroup_size: 512
    .name:           _Z9tg_kernelILi64ELi8ELi2ELb0EEvPKDF16_iS1_iPviPKf
    .private_segment_fixed_size: 0
    .sgpr_count:     22
    .sgpr_spill_count: 0
    .symbol:         _Z9tg_kernelILi64ELi8ELi2ELb0EEvPKDF16_iS1_iPviPKf.kd
    .uniform_work_group_size: 1
    .uses_dynamic_stack: false
    .vgpr_count:     62
    .vgpr_spill_count: 0
    .wavefront_size: 64
